# speedup vs baseline: 1.0263x; 1.0263x over previous
.Lh_no_out:
	s_cmp_eq_u32 s17, 0
	s_cselect_b32 s4, s4, s6
	s_cselect_b32 s5, s5, s7
	s_add_u32 s24, s8, s22
	s_addc_u32 s25, s9, 0
	s_add_u32 s4, s4, s21
	s_addc_u32 s5, s5, 0
	global_load_dwordx4 v[14:17], v18, s[24:25] nt
	global_load_dwordx4 v[2:5], v18, s[4:5] nt
	s_add_u32 s6, s4, 0x40000
	s_addc_u32 s7, s5, 0
	s_add_u32 s8, s4, 0x80000
	s_addc_u32 s9, s5, 0
	s_barrier
	global_load_dwordx4 v[6:9], v18, s[6:7] nt
	s_barrier
	global_load_dwordx4 v[10:13], v18, s[8:9] nt
	s_mul_i32 s46, s3, 0xc00
	s_add_u32 s46, s46, 0x8420
	v_lshl_add_u32 v26, v1, 2, s46
	v_and_b32_e32 v38, 15, v0
	s_mul_i32 s58, s17, 0x4200
	s_add_u32 s58, s58, 0x1e0
	v_lshl_add_u32 v38, v38, 2, s58
	v_add_u32_e32 v39, 0x1600, v38
	v_add_u32_e32 v40, 0x2c00, v38
	v_mov_b32_e32 v41, 0x41fc0000
	v_mov_b32_e32 v42, 0xbf38aa3b
	s_mov_b32 s48, 0x3f940000
	s_mov_b32 s51, 0x3fb8aa3b
	s_mov_b32 s42, 0
	s_mov_b32 s43, 0
	s_mov_b32 s44, 0x7fffffff
	s_mov_b32 s45, 0x7fffffff
	s_mov_b32 s47, 0
	s_mul_i32 s58, s3, 0x1600
	s_add_u32 s58, s58, 0x320
	v_lshl_add_u32 v44, v1, 6, s58
	v_bfe_u32 v45, v1, 2, 2
	v_lshlrev_b32_e32 v45, 4, v45
	v_xor_b32_e32 v46, 16, v45
	v_xor_b32_e32 v47, 32, v45
	v_xor_b32_e32 v48, 48, v45
	v_add_u32_e32 v45, v44, v45
	v_add_u32_e32 v46, v44, v46
	v_add_u32_e32 v47, v44, v47
	v_add_u32_e32 v48, v44, v48
	s_mul_i32 s58, s2, 0x600
	s_lshl_b32 s59, s3, 8
	s_add_u32 s58, s58, s59
	s_add_u32 s10, s10, s58
	s_addc_u32 s11, s11, 0
	v_lshlrev_b32_e32 v49, 2, v1
	s_lshl_b32 s58, s2, 2
	s_add_u32 s12, s12, s58
	s_addc_u32 s13, s13, 0
	s_setprio 3
	s_waitcnt vmcnt(3)
	v_cmp_lt_f32_e64 s[26:27], 0.5, v14
	v_cmp_lt_f32_e64 s[28:29], 0.5, v15
	v_cmp_lt_f32_e64 s[30:31], 0.5, v16
	v_cmp_lt_f32_e64 s[32:33], 0.5, v17
	s_cmp_lg_u32 s17, 0
	s_cbranch_scc1 .Lh_no_cnt
	s_bcnt1_i32_b64 s54, s[26:27]
	s_bcnt1_i32_b64 s55, s[28:29]
	s_bcnt1_i32_b64 s56, s[30:31]
	s_bcnt1_i32_b64 s57, s[32:33]
	s_add_i32 s54, s54, s55
	s_add_i32 s56, s56, s57
	s_add_i32 s54, s54, s56
	s_lshl_b32 s55, s16, 2
	v_mov_b32_e32 v36, s55
	v_mov_b32_e32 v37, s54
	s_mov_b64 exec, 1
	ds_write_b32 v36, v37
	s_mov_b64 exec, -1

.Lh_stage1:
	s_setprio 2
	s_mov_b32 s47, 1
	s_mov_b32 s44, s42
	s_waitcnt vmcnt(1)
	v_cmp_lt_f32_e64 s[34:35], |v6|, s48
	v_cmp_lt_f32_e64 s[36:37], |v7|, s48
	v_cmp_lt_f32_e64 s[38:39], |v8|, s48
	v_cmp_lt_f32_e64 s[40:41], |v9|, s48
	s_and_b64 s[34:35], s[34:35], s[26:27]
	s_and_b64 s[36:37], s[36:37], s[28:29]
	s_and_b64 s[38:39], s[38:39], s[30:31]
	s_and_b64 s[40:41], s[40:41], s[32:33]
	v_mbcnt_lo_u32_b32 v28, s34, 0
	v_mbcnt_lo_u32_b32 v29, s36, 0
	v_mbcnt_lo_u32_b32 v30, s38, 0
	v_mbcnt_lo_u32_b32 v31, s40, 0
	v_mbcnt_hi_u32_b32 v28, s35, v28
	v_mbcnt_hi_u32_b32 v29, s37, v29
	v_mbcnt_hi_u32_b32 v30, s39, v30
	v_mbcnt_hi_u32_b32 v31, s41, v31
	s_bcnt1_i32_b64 s54, s[34:35]
	s_bcnt1_i32_b64 s55, s[36:37]
	s_bcnt1_i32_b64 s56, s[38:39]
	s_bcnt1_i32_b64 s57, s[40:41]
	s_lshl2_add_u32 s58, s42, s46
	v_lshl_add_u32 v28, v28, 2, s58
	s_lshl2_add_u32 s58, s54, s58
	v_lshl_add_u32 v29, v29, 2, s58
	s_lshl2_add_u32 s58, s55, s58
	v_lshl_add_u32 v30, v30, 2, s58
	s_lshl2_add_u32 s58, s56, s58
	v_lshl_add_u32 v31, v31, 2, s58
	s_add_i32 s54, s54, s55
	s_add_i32 s56, s56, s57
	s_add_i32 s42, s42, s54
	s_add_i32 s42, s42, s56
	s_mov_b64 exec, s[34:35]
	ds_write_b32 v28, v6
	s_mov_b64 exec, s[36:37]
	ds_write_b32 v29, v7
	s_mov_b64 exec, s[38:39]
	ds_write_b32 v30, v8
	s_mov_b64 exec, s[40:41]
	ds_write_b32 v31, v9
	s_mov_b64 exec, -1
	s_branch .Lh_loop_entry
.Lh_stage2:
	s_setprio 1
	s_mov_b32 s47, 2
	s_mov_b32 s45, s42
	s_waitcnt vmcnt(0)
	v_cmp_lt_f32_e64 s[34:35], |v10|, s48
	v_cmp_lt_f32_e64 s[36:37], |v11|, s48
	v_cmp_lt_f32_e64 s[38:39], |v12|, s48
	v_cmp_lt_f32_e64 s[40:41], |v13|, s48
	s_and_b64 s[34:35], s[34:35], s[26:27]
	s_and_b64 s[36:37], s[36:37], s[28:29]
	s_and_b64 s[38:39], s[38:39], s[30:31]
	s_and_b64 s[40:41], s[40:41], s[32:33]
	v_mbcnt_lo_u32_b32 v28, s34, 0
	v_mbcnt_lo_u32_b32 v29, s36, 0
	v_mbcnt_lo_u32_b32 v30, s38, 0
	v_mbcnt_lo_u32_b32 v31, s40, 0
	v_mbcnt_hi_u32_b32 v28, s35, v28
	v_mbcnt_hi_u32_b32 v29, s37, v29
	v_mbcnt_hi_u32_b32 v30, s39, v30
	v_mbcnt_hi_u32_b32 v31, s41, v31
	s_bcnt1_i32_b64 s54, s[34:35]
	s_bcnt1_i32_b64 s55, s[36:37]
	s_bcnt1_i32_b64 s56, s[38:39]
	s_bcnt1_i32_b64 s57, s[40:41]
	s_lshl2_add_u32 s58, s42, s46
	v_lshl_add_u32 v28, v28, 2, s58
	s_lshl2_add_u32 s58, s54, s58
	v_lshl_add_u32 v29, v29, 2, s58
	s_lshl2_add_u32 s58, s55, s58
	v_lshl_add_u32 v30, v30, 2, s58
	s_lshl2_add_u32 s58, s56, s58
	v_lshl_add_u32 v31, v31, 2, s58
	s_add_i32 s54, s54, s55
	s_add_i32 s56, s56, s57
	s_add_i32 s42, s42, s54
	s_add_i32 s42, s42, s56
	s_mov_b64 exec, s[34:35]
	ds_write_b32 v28, v10
	s_mov_b64 exec, s[36:37]
	ds_write_b32 v29, v11
	s_mov_b64 exec, s[38:39]
	ds_write_b32 v30, v12
	s_mov_b64 exec, s[40:41]
	ds_write_b32 v31, v13
	s_mov_b64 exec, -1
	s_branch .Lh_loop_entry
.Lh_stage3:
	s_setprio 0
	s_mov_b32 s47, 3
	s_sub_i32 s59, s42, s43
	s_cmp_lt_i32 s59, 1
	s_cbranch_scc1 .Lh_epilogue
	s_bfm_b64 exec, s59, 0
	s_branch .Lh_loop_first
